# speedup vs baseline: 1.0418x; 1.0011x over previous
.LBB2_53:
	s_lshl_b32 s2, s41, 14
	s_waitcnt lgkmcnt(0)
	s_add_u32 s2, s26, s2
	s_addc_u32 s3, s27, 0
	s_add_u32 s4, s2, 0x1000
	s_addc_u32 s5, s3, 0
	s_add_u32 s6, s2, 0x2000
	s_addc_u32 s7, s3, 0
	s_add_u32 s8, s2, 0x3000
	s_addc_u32 s9, s3, 0
	v_lshlrev_b32_e32 v94, 4, v1
	v_lshlrev_b32_e32 v68, 4, v68
	v_lshl_or_b32 v94, s41, 8, v94
	global_load_dwordx4 v[86:89], v94, s[36:37] offset:0
	global_load_dwordx4 v[90:93], v94, s[24:25] offset:0
	global_load_dwordx4 v[2:5], v68, s[2:3]
	global_load_dwordx4 v[6:9], v68, s[2:3] offset:1024
	global_load_dwordx4 v[10:13], v68, s[2:3] offset:2048
	global_load_dwordx4 v[14:17], v68, s[2:3] offset:3072
	global_load_dwordx4 v[18:21], v68, s[4:5]
	global_load_dwordx4 v[22:25], v68, s[4:5] offset:1024
	global_load_dwordx4 v[26:29], v68, s[4:5] offset:2048
	global_load_dwordx4 v[30:33], v68, s[4:5] offset:3072
	global_load_dwordx4 v[34:37], v68, s[6:7]
	global_load_dwordx4 v[38:41], v68, s[6:7] offset:1024
	global_load_dwordx4 v[42:45], v68, s[6:7] offset:2048
	global_load_dwordx4 v[46:49], v68, s[6:7] offset:3072
	global_load_dwordx4 v[50:53], v68, s[8:9]
	global_load_dwordx4 v[54:57], v68, s[8:9] offset:1024
	global_load_dwordx4 v[58:61], v68, s[8:9] offset:2048
	global_load_dwordx4 v[62:65], v68, s[8:9] offset:3072
	v_mul_u32_u24_e32 v67, 0x410, v69
	v_and_b32_e32 v95, 48, v0
	s_lshl_b32 s8, s41, 8
	v_add3_u32 v67, s8, v67, v95
	s_lshl_b32 s4, s41, 7
	s_addk_i32 s4, 0x4100
	s_movk_i32 s5, 0x210
	v_lshlrev_b32_e32 v66, 3, v1
	v_add_u32_e32 v66, s4, v66
	v_mad_u32_u24 v66, v69, s5, v66
	s_mov_b32 s4, 0x3fb8aa3b
	s_mov_b32 s5, 0x3fb8aa3b
	s_mov_b32 s8, -1.0
	s_mov_b32 s9, -1.0
	s_lshl_b32 s2, s41, 13
	s_add_u32 s2, s16, s2
	s_addc_u32 s3, s17, 0
	s_add_u32 s6, s2, 0x1000
	s_addc_u32 s7, s3, 0
	s_barrier
	ds_read_b128 v[70:73], v67
	ds_read_b128 v[74:77], v67 offset:64
	ds_read_b128 v[78:81], v67 offset:128
	ds_read_b128 v[82:85], v67 offset:192
	s_waitcnt vmcnt(15) lgkmcnt(3)
	v_mfma_f32_16x16x32_f16 v[2:5], v[2:5], v[70:73], 0
	s_waitcnt vmcnt(14) lgkmcnt(2)
	v_mfma_f32_16x16x32_f16 v[2:5], v[6:9], v[74:77], v[2:5]
	s_waitcnt vmcnt(13) lgkmcnt(1)
	v_mfma_f32_16x16x32_f16 v[2:5], v[10:13], v[78:81], v[2:5]
	s_waitcnt vmcnt(12) lgkmcnt(0)
	v_mfma_f32_16x16x32_f16 v[2:5], v[14:17], v[82:85], v[2:5]
	global_load_dwordx4 v[6:9], v94, s[36:37] offset:64
	global_load_dwordx4 v[10:13], v94, s[24:25] offset:64
	s_waitcnt vmcnt(13)
	v_mfma_f32_16x16x32_f16 v[18:21], v[18:21], v[70:73], 0
	s_waitcnt vmcnt(12)
	v_mfma_f32_16x16x32_f16 v[18:21], v[22:25], v[74:77], v[18:21]
	s_waitcnt vmcnt(11)
	v_mfma_f32_16x16x32_f16 v[18:21], v[26:29], v[78:81], v[18:21]
	s_waitcnt vmcnt(10)
	v_mfma_f32_16x16x32_f16 v[18:21], v[30:33], v[82:85], v[18:21]
	global_load_dwordx4 v[22:25], v94, s[36:37] offset:128
	global_load_dwordx4 v[26:29], v94, s[24:25] offset:128
	v_pk_add_f32 v[2:3], v[2:3], v[86:87]
	v_pk_add_f32 v[4:5], v[4:5], v[88:89]
	v_pk_mul_f32 v[14:15], v[2:3], s[4:5]
	v_pk_mul_f32 v[16:17], v[4:5], s[4:5]
	v_exp_f32_e32 v14, v14
	v_exp_f32_e32 v15, v15
	v_exp_f32_e32 v16, v16
	v_exp_f32_e32 v17, v17
	v_cmp_lt_f32_e64 s[10:11], 0, v2
	v_cmp_lt_f32_e64 s[12:13], 0, v3
	v_cmp_lt_f32_e64 s[20:21], 0, v4
	v_cmp_lt_f32_e64 s[22:23], 0, v5
	v_pk_add_f32 v[14:15], v[14:15], s[8:9]
	v_pk_add_f32 v[16:17], v[16:17], s[8:9]
	v_cndmask_b32_e64 v2, v14, v2, s[10:11]
	v_cndmask_b32_e64 v3, v15, v3, s[12:13]
	v_cndmask_b32_e64 v4, v16, v4, s[20:21]
	v_cndmask_b32_e64 v5, v17, v5, s[22:23]
	v_pk_add_f32 v[2:3], v[2:3], v[90:91] neg_lo:[0,1] neg_hi:[0,1]
	v_pk_add_f32 v[4:5], v[4:5], v[92:93] neg_lo:[0,1] neg_hi:[0,1]
	v_cvt_pk_f16_f32 v14, v2, v3
	v_cvt_pk_f16_f32 v15, v4, v5
	ds_write_b64 v66, v[14:15] offset:0
	s_waitcnt vmcnt(11)
	v_mfma_f32_16x16x32_f16 v[34:37], v[34:37], v[70:73], 0
	s_waitcnt vmcnt(10)
	v_mfma_f32_16x16x32_f16 v[34:37], v[38:41], v[74:77], v[34:37]
	s_waitcnt vmcnt(9)
	v_mfma_f32_16x16x32_f16 v[34:37], v[42:45], v[78:81], v[34:37]
	s_waitcnt vmcnt(8)
	v_mfma_f32_16x16x32_f16 v[34:37], v[46:49], v[82:85], v[34:37]
	global_load_dwordx4 v[38:41], v94, s[36:37] offset:192
	global_load_dwordx4 v[42:45], v94, s[24:25] offset:192
	s_waitcnt vmcnt(9)
	v_mfma_f32_16x16x32_f16 v[50:53], v[50:53], v[70:73], 0
	s_waitcnt vmcnt(8)
	v_mfma_f32_16x16x32_f16 v[50:53], v[54:57], v[74:77], v[50:53]
	s_waitcnt vmcnt(7)
	v_mfma_f32_16x16x32_f16 v[50:53], v[58:61], v[78:81], v[50:53]
	s_waitcnt vmcnt(6)
	v_mfma_f32_16x16x32_f16 v[50:53], v[62:65], v[82:85], v[50:53]
	s_waitcnt vmcnt(4)
	v_pk_add_f32 v[18:19], v[18:19], v[6:7]
	v_pk_add_f32 v[20:21], v[20:21], v[8:9]
	v_pk_mul_f32 v[14:15], v[18:19], s[4:5]
	v_pk_mul_f32 v[16:17], v[20:21], s[4:5]
	v_exp_f32_e32 v14, v14
	v_exp_f32_e32 v15, v15
	v_exp_f32_e32 v16, v16
	v_exp_f32_e32 v17, v17
	v_cmp_lt_f32_e64 s[10:11], 0, v18
	v_cmp_lt_f32_e64 s[12:13], 0, v19
	v_cmp_lt_f32_e64 s[20:21], 0, v20
	v_cmp_lt_f32_e64 s[22:23], 0, v21
	v_pk_add_f32 v[14:15], v[14:15], s[8:9]
	v_pk_add_f32 v[16:17], v[16:17], s[8:9]
	v_cndmask_b32_e64 v18, v14, v18, s[10:11]
	v_cndmask_b32_e64 v19, v15, v19, s[12:13]
	v_cndmask_b32_e64 v20, v16, v20, s[20:21]
	v_cndmask_b32_e64 v21, v17, v21, s[22:23]
	v_pk_add_f32 v[18:19], v[18:19], v[10:11] neg_lo:[0,1] neg_hi:[0,1]
	v_pk_add_f32 v[20:21], v[20:21], v[12:13] neg_lo:[0,1] neg_hi:[0,1]
	v_cvt_pk_f16_f32 v14, v18, v19
	v_cvt_pk_f16_f32 v15, v20, v21
	ds_write_b64 v66, v[14:15] offset:32
	global_load_dwordx4 v[2:5], v68, s[2:3]
	global_load_dwordx4 v[6:9], v68, s[2:3] offset:1024
	global_load_dwordx4 v[10:13], v68, s[2:3] offset:2048
	global_load_dwordx4 v[14:17], v68, s[2:3] offset:3072
	global_load_dwordx4 v[18:21], v68, s[6:7]
	s_waitcnt vmcnt(7)
	v_pk_add_f32 v[34:35], v[34:35], v[22:23]
	v_pk_add_f32 v[36:37], v[36:37], v[24:25]
	v_pk_mul_f32 v[46:47], v[34:35], s[4:5]
	v_pk_mul_f32 v[48:49], v[36:37], s[4:5]
	v_exp_f32_e32 v46, v46
	v_exp_f32_e32 v47, v47
	v_exp_f32_e32 v48, v48
	v_exp_f32_e32 v49, v49
	v_cmp_lt_f32_e64 s[10:11], 0, v34
	v_cmp_lt_f32_e64 s[12:13], 0, v35
	v_cmp_lt_f32_e64 s[20:21], 0, v36
	v_cmp_lt_f32_e64 s[22:23], 0, v37
	v_pk_add_f32 v[46:47], v[46:47], s[8:9]
	v_pk_add_f32 v[48:49], v[48:49], s[8:9]
	v_cndmask_b32_e64 v34, v46, v34, s[10:11]
	v_cndmask_b32_e64 v35, v47, v35, s[12:13]
	v_cndmask_b32_e64 v36, v48, v36, s[20:21]
	v_cndmask_b32_e64 v37, v49, v37, s[22:23]
	v_pk_add_f32 v[34:35], v[34:35], v[26:27] neg_lo:[0,1] neg_hi:[0,1]
	v_pk_add_f32 v[36:37], v[36:37], v[28:29] neg_lo:[0,1] neg_hi:[0,1]
	v_cvt_pk_f16_f32 v46, v34, v35
	v_cvt_pk_f16_f32 v47, v36, v37
	ds_write_b64 v66, v[46:47] offset:64
	global_load_dwordx4 v[22:25], v68, s[6:7] offset:1024
	global_load_dwordx4 v[26:29], v68, s[6:7] offset:2048
	global_load_dwordx4 v[30:33], v68, s[6:7] offset:3072
	s_waitcnt vmcnt(8)
	v_pk_add_f32 v[50:51], v[50:51], v[38:39]
	v_pk_add_f32 v[52:53], v[52:53], v[40:41]
	v_pk_mul_f32 v[46:47], v[50:51], s[4:5]
	v_pk_mul_f32 v[48:49], v[52:53], s[4:5]
	v_exp_f32_e32 v46, v46
	v_exp_f32_e32 v47, v47
	v_exp_f32_e32 v48, v48
	v_exp_f32_e32 v49, v49
	v_cmp_lt_f32_e64 s[10:11], 0, v50
	v_cmp_lt_f32_e64 s[12:13], 0, v51
	v_cmp_lt_f32_e64 s[20:21], 0, v52
	v_cmp_lt_f32_e64 s[22:23], 0, v53
	v_pk_add_f32 v[46:47], v[46:47], s[8:9]
	v_pk_add_f32 v[48:49], v[48:49], s[8:9]
	v_cndmask_b32_e64 v50, v46, v50, s[10:11]
	v_cndmask_b32_e64 v51, v47, v51, s[12:13]
	v_cndmask_b32_e64 v52, v48, v52, s[20:21]
	v_cndmask_b32_e64 v53, v49, v53, s[22:23]
	v_pk_add_f32 v[50:51], v[50:51], v[42:43] neg_lo:[0,1] neg_hi:[0,1]
	v_pk_add_f32 v[52:53], v[52:53], v[44:45] neg_lo:[0,1] neg_hi:[0,1]
	v_cvt_pk_f16_f32 v46, v50, v51
	v_cvt_pk_f16_f32 v47, v52, v53
	ds_write_b64 v66, v[46:47] offset:96
	v_mul_u32_u24_e32 v35, 0x210, v69
	v_lshl_or_b32 v34, v1, 2, 1
	v_add_u32_e32 v35, v35, v95
	s_waitcnt lgkmcnt(0)
	s_barrier
	ds_read_b128 v[36:39], v35 offset:16640
	ds_read_b128 v[40:43], v35 offset:16704
	s_movk_i32 s2, 0x440
	s_waitcnt vmcnt(7) lgkmcnt(1)
	v_mfma_f32_16x16x32_f16 v[2:5], v[36:39], v[2:5], 0
	ds_read_b128 v[36:39], v35 offset:16768
	s_waitcnt vmcnt(6) lgkmcnt(1)
	v_mfma_f32_16x16x32_f16 v[2:5], v[40:43], v[6:9], v[2:5]
	ds_read_b128 v[6:9], v35 offset:16832
	s_waitcnt vmcnt(5) lgkmcnt(1)
	v_mfma_f32_16x16x32_f16 v[2:5], v[36:39], v[10:13], v[2:5]
	ds_read_b128 v[10:13], v35 offset:16896
	s_waitcnt vmcnt(4) lgkmcnt(1)
	v_mfma_f32_16x16x32_f16 v[2:5], v[6:9], v[14:17], v[2:5]
	ds_read_b128 v[6:9], v35 offset:16960
	s_waitcnt vmcnt(3) lgkmcnt(1)
	v_mfma_f32_16x16x32_f16 v[2:5], v[10:13], v[18:21], v[2:5]
	ds_read_b128 v[10:13], v35 offset:17024
	s_waitcnt vmcnt(2) lgkmcnt(1)
	v_mfma_f32_16x16x32_f16 v[2:5], v[6:9], v[22:25], v[2:5]
	ds_read_b128 v[6:9], v35 offset:17088
	s_waitcnt vmcnt(1) lgkmcnt(1)
	v_mfma_f32_16x16x32_f16 v[2:5], v[10:13], v[26:29], v[2:5]
	s_waitcnt vmcnt(0) lgkmcnt(0)
	v_mfma_f32_16x16x32_f16 v[2:5], v[6:9], v[30:33], v[2:5]
	v_lshlrev_b32_e32 v6, 2, v69
	v_lshl_or_b32 v7, s41, 6, v6
	v_mad_u32_u24 v1, v1, s2, v7
	s_movk_i32 s2, 0x110
	s_nop 3
	ds_write_b32 v1, v2
	v_mad_u32_u24 v1, v34, s2, v7
	v_lshlrev_b32_e32 v2, 4, v69
	ds_write2_b32 v1, v3, v4 offset1:68
	ds_write_b32 v1, v5 offset:544
	s_waitcnt lgkmcnt(0)
	global_load_dwordx4 v[8:11], v2, s[24:25] offset:1024
	global_load_dwordx4 v[12:15], v2, s[18:19]
	global_load_dwordx4 v[16:19], v2, s[14:15]
	v_lshrrev_b32_e32 v1, 4, v0
	v_mad_u32_u24 v2, v1, s2, v2
	s_barrier
	ds_read_b128 v[2:5], v2
	s_movk_i32 s2, 0x100
	s_waitcnt vmcnt(2) lgkmcnt(0)
	v_add_f32_e32 v9, v3, v9
	v_add_f32_e32 v8, v2, v8
	s_waitcnt vmcnt(1)
	v_mul_f32_e32 v13, v13, v9
	s_waitcnt vmcnt(0)
	v_mul_f32_e32 v9, v17, v9
	v_add_f32_e32 v10, v4, v10
	v_fmac_f32_e32 v13, v12, v8
	v_fmac_f32_e32 v9, v16, v8
	v_add_f32_e32 v11, v5, v11
	v_fmac_f32_e32 v13, v14, v10
	v_fmac_f32_e32 v9, v18, v10
	v_fmac_f32_e32 v13, v15, v11
	v_fmac_f32_e32 v9, v19, v11
	s_nop 1
	v_add_f32_dpp v13, v13, v13 row_mirror row_mask:0xf bank_mask:0xf
	v_add_f32_dpp v9, v9, v9 row_mirror row_mask:0xf bank_mask:0xf
	s_nop 0
	v_add_f32_dpp v13, v13, v13 row_half_mirror row_mask:0xf bank_mask:0xf
	v_add_f32_dpp v9, v9, v9 row_half_mirror row_mask:0xf bank_mask:0xf
	s_nop 0
	v_add_f32_dpp v13, v13, v13 quad_perm:[2,3,0,1] row_mask:0xf bank_mask:0xf
	v_add_f32_dpp v9, v9, v9 quad_perm:[2,3,0,1] row_mask:0xf bank_mask:0xf
	s_nop 0
	v_add_f32_dpp v7, v13, v13 quad_perm:[1,0,3,2] row_mask:0xf bank_mask:0xf
	v_add_f32_dpp v12, v9, v9 quad_perm:[1,0,3,2] row_mask:0xf bank_mask:0xf
	v_cmp_gt_u32_e32 vcc, s2, v0
	s_and_saveexec_b64 s[2:3], vcc
	s_cbranch_execz .LBB2_57
	v_lshlrev_b32_e32 v0, 2, v1
	ds_read_b32 v0, v0 offset:25152
	s_load_dwordx2 s[2:3], s[0:1], 0x50
	v_cmp_eq_u32_e32 vcc, 0, v69
	s_waitcnt lgkmcnt(0)
	v_add_u32_e32 v0, s33, v0
	v_ashrrev_i32_e32 v1, 31, v0
	s_and_saveexec_b64 s[4:5], vcc
	s_cbranch_execz .LBB2_56
	s_load_dwordx4 s[8:11], s[0:1], 0x58
	v_lshlrev_b64 v[8:9], 2, v[0:1]
	s_waitcnt lgkmcnt(0)
	v_lshl_add_u64 v[10:11], s[10:11], 0, v[8:9]
	v_lshl_add_u64 v[8:9], s[8:9], 0, v[8:9]
	global_store_dword v[8:9], v7, off
	global_store_dword v[10:11], v12, off

.LBB2_57:
	s_endpgm
	s_nop 0
	s_nop 0
	s_nop 0
	s_nop 0
	s_nop 0
	s_nop 0
	s_nop 0
	s_nop 0
	s_nop 0
	s_nop 0
	s_nop 0
	s_nop 0
	s_nop 0
	s_nop 0
	s_nop 0
	s_nop 0
	s_nop 0
	s_nop 0
	s_nop 0
	s_nop 0
	s_nop 0
	s_nop 0
	s_nop 0
	s_nop 0
	s_nop 0
	s_nop 0
	s_nop 0
	s_nop 0
	s_nop 0
	s_nop 0
	s_nop 0
	s_nop 0
	s_nop 0
	s_nop 0
	s_nop 0
	s_endpgm
